# split 12 attention / 12 top-k (every 2nd token) / 0 phase 2
# speedup vs baseline: 1.0131x; 1.0131x over previous
; #define LAS __attribute__((address_space(3)))
; __device__ __forceinline__ void convert_experts(Frame& F, int lo, int hi) {
;     const int gw = F.vcu * 8 + F.wave, NGW = F.G * 8;
;     LAS unsigned char* scr = F.lds + F.wave * 16384;
;     unsigned char* W1t = WSP(F, WS_W1T, unsigned char); unsigned char* W2t = WSP(F, WS_W2T, unsigned char);
;     const float* weg = F.a->in[I_WEG]; const float* weu = F.a->in[I_WEU]; const float* wed = F.a->in[I_WED];
;     const float* wsg = F.a->in[I_WSG]; const float* wsu = F.a->in[I_WSU]; const float* wsd = F.a->in[I_WSD];
;     ...
;     constexpr int NPAIRS = CONV_ITEMS / 2;
;     (void)lo; (void)hi;
;     ...
;     if (gw < NPAIRS) {
;         const int ns = 2 * ((NPAIRS - gw + NGW - 1) / NGW);
;         int sq = 0, r = CONV_RIDX(0);
; __device__ __forceinline__ void router_topk(Frame& F, int tile) {
;     const float* logits = WSP(F, WS_B, float); const float* br = F.a->in[I_BR];
;     int* tk_e = WSP(F, WS_TOPK_E, int); float* tk_g = WSP(F, WS_TOPK_G, float); int* tk_p = WSP(F, WS_TOPK_P, int);
;     int* gcnt = (int*)(F.a->ws + WS_CTL + CTL_CNT);
;     LAS int* hist = (LAS int*)F.lds; LAS int* base = hist + 256;
;     const int lane = F.lane, w = F.wave;
;     if (F.tid < 256) hist[F.tid] = 0;
;     __syncthreads();
;     const f32x4 bias = *(const f32x4*)(br + 4 * lane);
;     f32x4 lgn = *(const f32x4*)(logits + (size_t)(tile * 256 + w * 32) * 256 + 4 * lane);
;     int pe = 0, pp = 0; float pg = 0.f;
;     int* dumpi = (int*)(F.a->ws + WS_B + ((size_t)128 << 20));
.Lcvt_vcu:
	s_add_u32 s69, s41, s40
	s_and_b32 s69, s69, 1
	s_lshl_b32 s41, s41, 3
	s_add_u32 s89, s41, s40
	s_lshl_b32 s71, s64, 3
	s_mul_i32 s39, s71, 12
	s_add_u32 s89, s89, s39
	s_movk_i32 s90, 12
	s_mov_b32 s32, 0
	s_add_u32 s86, s84, 0x9180000
	s_addc_u32 s87, s85, 0
	s_add_u32 s84, s84, 0x1100000
	s_addc_u32 s85, s85, 0
	s_add_u32 s14, s8, 0x900000
	s_addc_u32 s15, s9, 0
	s_add_u32 s16, s8, 0xb00000
	s_addc_u32 s17, s9, 0
	s_add_u32 s18, s8, 0xd00000
	s_addc_u32 s19, s9, 0
	v_mov_b32_e32 v131, 0
	s_add_u32 s20, s8, 0x4000
	v_mov_b32_e32 v133, v131
	s_addc_u32 s21, s9, 0
	v_lshl_add_u64 v[2:3], s[8:9], 0, v[132:133]
	s_mov_b64 s[8:9], 0x1d1c0000
	s_waitcnt vmcnt(0)
	v_lshl_add_u64 v[12:13], v[2:3], 0, s[8:9]
	s_mov_b64 s[8:9], 0x1d1c0100
	s_movk_i32 s4, 0x100
	v_mov_b32_e32 v135, v131
	v_lshl_add_u64 v[14:15], v[2:3], 0, s[8:9]
	s_mov_b64 s[8:9], 0x1d1c0200
	v_cmp_gt_i32_e64 s[4:5], s4, v1
	s_mov_b32 s26, 0
	v_lshl_add_u32 v22, v1, 2, 0
	s_lshl_b32 s27, s49, 5
	v_lshl_add_u64 v[10:11], s[6:7], 0, v[134:135]
	v_cmp_gt_u32_e64 s[6:7], 8, v130
	v_lshl_add_u64 v[16:17], v[2:3], 0, s[8:9]
	v_mov_b64_e32 v[18:19], 0x100
	v_mov_b64_e32 v[20:21], 0xff
	v_mov_b32_e32 v23, 0xff800000
	v_mov_b32_e32 v24, 1
	s_waitcnt vmcnt(0)
	s_barrier
	s_branch .LBB0_532

; __device__ __forceinline__ void router_topk(Frame& F, int tile) {
;     ...
;     for (int i = 0; i < 32; ++i) {
;         const int tok = tile * 256 + w * 32 + i;
;         const f32x4 lg = lgn;
;         {
;           const bool real = lane < 8 && i > 0; const size_t o = (size_t)(tok - 1) * 8 + lane;
;           int* de = real ? tk_e + o : dumpi + lane; float* dg = real ? tk_g + o : (float*)dumpi + 64 + lane; int* dp = real ? tk_p + o : dumpi + 128 + lane;
;           *de = pe; *dg = pg; *dp = pp; }
;         lgn = *(const f32x4*)(logits + (size_t)(i + 1 < 32 ? tok + 1 : tok) * 256 + 4 * lane);
.Lcvt_wd:
	v_mov_b64_e32 v[30:31], v[8:9]
	s_cmp_lg_u32 s24, 31
	v_mov_b64_e32 v[28:29], v[6:7]
	v_lshl_add_u64 v[6:7], s[30:31], 0, v[130:131]
	s_cselect_b64 s[30:31], -1, 0
	v_lshlrev_b64 v[6:7], 2, v[6:7]
	s_cmp_lg_u64 s[30:31], 0
	v_lshl_add_u64 v[8:9], s[14:15], 0, v[6:7]
	v_lshl_add_u64 v[32:33], s[16:17], 0, v[6:7]
	v_lshl_add_u64 v[6:7], s[18:19], 0, v[6:7]
	s_addc_u32 s8, s8, 0
	v_cndmask_b32_e32 v9, v13, v9, vcc
	v_cndmask_b32_e32 v8, v12, v8, vcc
	v_cndmask_b32_e32 v6, v16, v6, vcc
	s_ashr_i32 s9, s8, 31
	v_cndmask_b32_e32 v33, v15, v33, vcc
	v_cndmask_b32_e32 v32, v14, v32, vcc
	v_cndmask_b32_e32 v7, v17, v7, vcc
	global_store_dword v[8:9], v27, off
	global_store_dword v[32:33], v26, off
	s_waitcnt lgkmcnt(0)
	global_store_dword v[6:7], v25, off
	v_mul_f32_e32 v6, 0xbfb8aa3b, v28
	s_lshl_b64 s[8:9], s[8:9], 10
	v_exp_f32_e32 v28, v6
	v_lshl_add_u64 v[6:7], v[10:11], 0, s[8:9]
	global_load_dwordx4 v[6:9], v[6:7], off
	s_sub_u32 s69, s69, 1
	s_cmp_lt_i32 s69, 0
	s_cbranch_scc0 .Lcvt_none_l
	s_mov_b32 s69, 1
	s_cmp_eq_u32 s90, 0
	s_cbranch_scc1 .Lcvt_none_l
	s_cmp_lg_u32 s32, 0
	s_cbranch_scc1 .Lcvt_none_l
	s_sub_u32 s90, s90, 1
	s_lshr_b32 s39, s89, 6
	s_and_b32 s40, s89, 63
	s_mul_hi_u32 s42, s39, 0xaaaaaaab
	s_lshr_b32 s42, s42, 1
	s_mul_i32 s41, s42, 3
	s_sub_u32 s41, s39, s41
	s_cmp_lt_u32 s42, 256
	s_cselect_b32 s100, s42, 0
	s_cselect_b64 s[44:45], -1, 0
	s_lshl_b32 s100, s100, 20
	s_cmp_eq_u32 s41, 2
	s_cbranch_scc1 .Lcvt_down_l
	s_cmp_eq_u32 s41, 0
	s_cselect_b64 s[96:97], s[72:73], s[74:75]
	s_cselect_b64 s[98:99], s[78:79], s[80:81]
	s_mov_b32 s94, 0xc3317218
	s_cselect_b32 s94, 0xc2b8aa3b, s94
	s_cmp_lg_u64 s[44:45], 0
	s_cselect_b64 s[96:97], s[96:97], s[98:99]
	s_lshr_b32 s55, s40, 3
	s_and_b32 s58, s40, 7
	s_lshl_b32 s39, s55, 17
	s_add_u32 s100, s100, s39
	s_lshl_b32 s39, s58, 7
	s_add_u32 s100, s100, s39
	s_add_u32 s96, s96, s100
	s_addc_u32 s97, s97, 0
	s_lshl_b32 s42, s42, 19
	s_lshr_b32 s39, s58, 2
	s_lshl_b32 s39, s39, 18
	s_add_u32 s42, s42, s39
	s_and_b32 s39, s58, 3
	s_lshl_b32 s39, s39, 15
	s_add_u32 s42, s42, s39
	s_lshl_b32 s39, s41, 17
	s_add_u32 s42, s42, s39
	s_lshl_b32 s39, s55, 7
	s_add_u32 s42, s42, s39
	s_add_u32 s92, s84, s42
	s_addc_u32 s93, s85, 0
	s_movk_i32 s36, 0x400
	s_movk_i32 s38, 0x1000
	s_movk_i32 s98, 0x400
	s_branch .Lcvt_go_l
